# diff attention softmax chain: lane^32 max exchange by v_permlane32_swap instead of ds_bpermute, LDS wait moved to the first PV MFMA
# speedup vs baseline: 1.0033x; 1.0009x over previous
; #define LAS __attribute__((address_space(3)))
; #define AT_SCHED() __builtin_amdgcn_sched_barrier(0)
; template <int NDT>
; __device__ __forceinline__ void pv32(const f16x8* vf, const f32x16& p, f32x16 (&o)[NDT]) {
; #pragma unroll
;     for (int s2 = 0; s2 < 2; ++s2) {
;         f16x8 pb;
; #pragma unroll
;         for (int j = 0; j < 8; ++j) pb[j] = (f16)p[8 * s2 + j];
; #pragma unroll
;         for (int dt = 0; dt < NDT; ++dt) o[dt] = __builtin_amdgcn_mfma_f32_32x32x16_f16(vf[s2 * NDT + dt], pb, o[dt], 0, 0, 0);
;     }
; }
;     if (__any(d != 0.f)) {
; #pragma unroll
;         for (int r = 0; r < 16; ++r) s[r] -= d; }
; #pragma unroll
;     for (int r = 0; r < 16; ++r) { s[r] = __builtin_amdgcn_exp2f(s[r]); ps += s[r]; }
;     return ps; }
; template <int NDT>
; __device__ __forceinline__ void step64(LAS unsigned char* slot, const Addr<NDT>& a, const f16x8 (&qf)[4], f32x16 (&o)[NDT], float& m, float& l, f32x16& negm, bool& started) {
;     f16x8 kf[8], va[2 * NDT], vb[2 * NDT];
;     load_k<NDT>(slot, a, 0, kf); load_k<NDT>(slot, a, 8192, kf + 4);
;     load_v<NDT>(slot, a, 0, va);
;     AT_SCHED();
;     f32x16 s0 = qk32(kf, qf, negm), s1 = qk32(kf + 4, qf, negm);
;     AT_SCHED();
;     load_v<NDT>(slot, a, 8192, vb);
;     float mx = fmaxf(rowmax16(s0), rowmax16(s1)); mx = fmaxf(mx, __shfl_xor(mx, 32));
;     const float d = rescale<NDT>(mx, m, l, o, negm, started);
;     l += expsum(s0, d) + expsum(s1, d);
;     AT_SCHED();
;     pv32<NDT>(va, s0, o); pv32<NDT>(vb, s1, o);
;     AT_SCHED();
; }
.LBB0_549:
	v_exp_f32_e32 v2, v114
	v_exp_f32_e32 v244, v98
	v_exp_f32_e32 v233, v115
	v_exp_f32_e32 v245, v99
	v_exp_f32_e32 v242, v116
	v_exp_f32_e32 v246, v100
	v_exp_f32_e32 v243, v117
	v_exp_f32_e32 v247, v101
	v_add_f32_e32 v16, 0, v2
	v_exp_f32_e32 v114, v118
	v_add_f32_e32 v17, 0, v244
	v_exp_f32_e32 v115, v102
	v_add_f32_e32 v16, v233, v16
	v_exp_f32_e32 v116, v119
	v_add_f32_e32 v17, v245, v17
	v_exp_f32_e32 v117, v103
	v_add_f32_e32 v16, v242, v16
	v_exp_f32_e32 v118, v120
	v_add_f32_e32 v17, v246, v17
	v_exp_f32_e32 v119, v104
	v_add_f32_e32 v16, v243, v16
	v_exp_f32_e32 v120, v121
	v_add_f32_e32 v17, v247, v17
	v_exp_f32_e32 v121, v105
	v_exp_f32_e32 v122, v122
	v_exp_f32_e32 v234, v123
	v_exp_f32_e32 v123, v106
	v_pk_add_f32 v[16:17], v[114:115], v[16:17]
	v_exp_f32_e32 v235, v107
	v_pk_add_f32 v[16:17], v[116:117], v[16:17]
	v_exp_f32_e32 v124, v124
	v_exp_f32_e32 v236, v125
	v_exp_f32_e32 v125, v108
	v_pk_add_f32 v[16:17], v[118:119], v[16:17]
	v_exp_f32_e32 v237, v109
	v_pk_add_f32 v[16:17], v[120:121], v[16:17]
	v_exp_f32_e32 v126, v126
	v_exp_f32_e32 v238, v127
	v_exp_f32_e32 v127, v110
	v_pk_add_f32 v[16:17], v[122:123], v[16:17]
	v_exp_f32_e32 v239, v111
	v_pk_add_f32 v[16:17], v[234:235], v[16:17]
	v_exp_f32_e32 v128, v128
	v_exp_f32_e32 v240, v129
	v_exp_f32_e32 v129, v112
	v_pk_add_f32 v[16:17], v[124:125], v[16:17]
	v_exp_f32_e32 v241, v113
	v_pk_add_f32 v[16:17], v[236:237], v[16:17]
	s_nop 0
	v_pk_add_f32 v[16:17], v[126:127], v[16:17]
	s_nop 0
	v_pk_add_f32 v[16:17], v[238:239], v[16:17]
	s_nop 0
	v_pk_add_f32 v[16:17], v[128:129], v[16:17]
	s_nop 0
	v_pk_add_f32 v[16:17], v[240:241], v[16:17]
	s_nop 0
	v_add_f32_e32 v16, v16, v17
	v_add_f32_e32 v231, v231, v16
	v_cvt_pk_f16_f32 v101, v118, v120
	v_cvt_pk_f16_f32 v100, v114, v116
	v_cvt_pk_f16_f32 v99, v242, v243
	v_cvt_pk_f16_f32 v98, v2, v233
	s_waitcnt lgkmcnt(0)
	s_nop 1
	v_mfma_f32_32x32x16_f16 v[66:81], v[154:157], v[98:101], v[66:81]
	v_mfma_f32_32x32x16_f16 v[50:65], v[166:169], v[98:101], v[50:65]
	v_mfma_f32_32x32x16_f16 v[34:49], v[174:177], v[98:101], v[34:49]
	v_mfma_f32_32x32x16_f16 v[18:33], v[178:181], v[98:101], v[18:33]
	v_cvt_pk_f16_f32 v101, v128, v240
	v_cvt_pk_f16_f32 v100, v126, v238
	v_cvt_pk_f16_f32 v99, v124, v236
	v_cvt_pk_f16_f32 v98, v122, v234
	s_nop 1
	v_mfma_f32_32x32x16_f16 v[66:81], v[4:7], v[98:101], v[66:81]
	v_cvt_pk_f16_f32 v7, v119, v121
	v_cvt_pk_f16_f32 v6, v115, v117
	v_cvt_pk_f16_f32 v5, v246, v247
	v_cvt_pk_f16_f32 v4, v244, v245
	v_mfma_f32_32x32x16_f16 v[50:65], v[8:11], v[98:101], v[50:65]
	v_mfma_f32_32x32x16_f16 v[34:49], v[12:15], v[98:101], v[34:49]
	v_mfma_f32_32x32x16_f16 v[18:33], v[146:149], v[98:101], v[18:33]
	v_mfma_f32_32x32x16_f16 v[66:81], v[170:173], v[4:7], v[66:81]
	v_mfma_f32_32x32x16_f16 v[50:65], v[182:185], v[4:7], v[50:65]
	v_mfma_f32_32x32x16_f16 v[34:49], v[186:189], v[4:7], v[34:49]
	v_mfma_f32_32x32x16_f16 v[18:33], v[194:197], v[4:7], v[18:33]
	v_cvt_pk_f16_f32 v7, v129, v241
	v_cvt_pk_f16_f32 v6, v127, v239
	v_cvt_pk_f16_f32 v5, v125, v237
	v_cvt_pk_f16_f32 v4, v123, v235
	s_nop 1
	v_mfma_f32_32x32x16_f16 v[66:81], v[150:153], v[4:7], v[66:81]
	v_mfma_f32_32x32x16_f16 v[50:65], v[158:161], v[4:7], v[50:65]
	v_mfma_f32_32x32x16_f16 v[34:49], v[162:165], v[4:7], v[34:49]
	v_mfma_f32_32x32x16_f16 v[18:33], v[190:193], v[4:7], v[18:33]
	s_add_i32 s18, s18, 1
	s_add_i32 s19, s19, 0x8000
	s_add_i32 s20, s20, 64
	s_cmp_eq_u32 s19, 0x138000
	s_cbranch_scc1 .LBB0_572

; #define LAS __attribute__((address_space(3)))
; #define AT_SCHED() __builtin_amdgcn_sched_barrier(0)
; __device__ __forceinline__ float max3f(float a, float b, float c) { float r; asm("v_max3_f32 %0, %1, %2, %3" : "=v"(r) : "v"(a), "v"(b), "v"(c)); return r; }
; __device__ __forceinline__ float rowmax16(const f32x16& s) { float a = max3f(s[0], s[1], s[2]), b = max3f(s[3], s[4], s[5]);
;     a = max3f(a, s[6], s[7]); b = max3f(b, s[8], s[9]); a = max3f(a, s[10], s[11]); b = max3f(b, s[12], s[13]); a = max3f(a, s[14], s[15]); return fmaxf(a, b); }
; template <int NDT>
; __device__ __forceinline__ float rescale(float mx, float& m, float& l, f32x16 (&o)[NDT], f32x16& negm, bool& started) {
;     const bool quiet = started ? (mx <= THR) : (mx == -INFINITY);
;     if (__all(quiet)) return 0.f;
;     float d = 0.f, alpha = 1.f;
;     if (started) { d = fmaxf(mx, 0.f); alpha = __builtin_amdgcn_exp2f(-d); }
;     else if (mx > -INFINITY) { d = mx; started = true; }
;     m += d; l *= alpha;
; #pragma unroll
;     for (int dt = 0; dt < NDT; ++dt)
; #pragma unroll
;         for (int r = 0; r < 16; ++r) o[dt][r] *= alpha;
; #pragma unroll
;     for (int r = 0; r < 16; ++r) negm[r] = -m;
;     return d;
; }
;     if (__any(d != 0.f)) {
; #pragma unroll
;         for (int r = 0; r < 16; ++r) s[r] -= d; }
; #pragma unroll
;     for (int r = 0; r < 16; ++r) { s[r] = __builtin_amdgcn_exp2f(s[r]); ps += s[r]; }
;     return ps; }
; template <int NDT>
; __device__ __forceinline__ void step64(LAS unsigned char* slot, const Addr<NDT>& a, const f16x8 (&qf)[4], f32x16 (&o)[NDT], float& m, float& l, f32x16& negm, bool& started) {
;     f16x8 kf[8], va[2 * NDT], vb[2 * NDT];
;     load_k<NDT>(slot, a, 0, kf); load_k<NDT>(slot, a, 8192, kf + 4);
;     load_v<NDT>(slot, a, 0, va);
;     AT_SCHED();
;     f32x16 s0 = qk32(kf, qf, negm), s1 = qk32(kf + 4, qf, negm);
;     AT_SCHED();
;     load_v<NDT>(slot, a, 8192, vb);
;     float mx = fmaxf(rowmax16(s0), rowmax16(s1)); mx = fmaxf(mx, __shfl_xor(mx, 32));
;     const float d = rescale<NDT>(mx, m, l, o, negm, started);
.LBB0_560:
	s_add_i32 s3, s19, 0xfffe8000
	s_and_b32 s3, s3, 0x18000
	s_add_i32 s3, s3, 0
	v_add_u32_e32 v2, s3, v219
	v_add_u32_e32 v4, s3, v221
	v_add_u32_e32 v5, s3, v220
	v_add_u32_e32 v6, s3, v222
	ds_read_b128 v[98:101], v2
	ds_read_b128 v[150:153], v2 offset:8192
	ds_read_b128 v[102:105], v4
	ds_read_b128 v[158:161], v4 offset:8192
	ds_read_b128 v[106:109], v5
	ds_read_b128 v[162:165], v5 offset:8192
	ds_read_b128 v[110:113], v6
	ds_read_b128 v[170:173], v6 offset:8192
	v_add_u32_e32 v2, s3, v223
	v_add_u32_e32 v16, s3, v224
	v_add_u32_e32 v17, s3, v225
	v_add_u32_e32 v186, s3, v226
	v_add_u32_e32 v190, s3, v227
	v_add_u32_e32 v191, s3, v228
	v_add_u32_e32 v233, s3, v229
	v_add_u32_e32 v192, s3, v230
	ds_read_b64_tr_b16 v[154:155], v2 offset:16384
	ds_read_b64_tr_b16 v[156:157], v16 offset:16384
	ds_read_b64_tr_b16 v[6:7], v16 offset:20480
	ds_read_b64_tr_b16 v[4:5], v2 offset:20480
	ds_read_b64_tr_b16 v[166:167], v17 offset:16384
	ds_read_b64_tr_b16 v[168:169], v186 offset:16384
	ds_read_b64_tr_b16 v[10:11], v186 offset:20480
	ds_read_b64_tr_b16 v[8:9], v17 offset:20480
	ds_read_b64_tr_b16 v[174:175], v190 offset:16384
	ds_read_b64_tr_b16 v[176:177], v191 offset:16384
	ds_read_b64_tr_b16 v[14:15], v191 offset:20480
	ds_read_b64_tr_b16 v[12:13], v190 offset:20480
	ds_read_b64_tr_b16 v[178:179], v233 offset:16384
	ds_read_b64_tr_b16 v[180:181], v192 offset:16384
	ds_read_b64_tr_b16 v[148:149], v192 offset:20480
	ds_read_b64_tr_b16 v[146:147], v233 offset:20480
	s_waitcnt lgkmcnt(14)
	v_mfma_f32_32x32x16_f16 v[114:129], v[98:101], v[142:145], v[82:97]
	v_mfma_f32_32x32x16_f16 v[114:129], v[102:105], v[138:141], v[114:129]
	v_mfma_f32_32x32x16_f16 v[114:129], v[106:109], v[134:137], v[114:129]
	v_mfma_f32_32x32x16_f16 v[114:129], v[110:113], v[130:133], v[114:129]
	v_mov_b64_e32 v[112:113], v[96:97]
	v_mov_b64_e32 v[110:111], v[94:95]
	v_mov_b64_e32 v[108:109], v[92:93]
	v_mov_b64_e32 v[106:107], v[90:91]
	v_mov_b64_e32 v[104:105], v[88:89]
	v_mov_b64_e32 v[102:103], v[86:87]
	v_mov_b64_e32 v[100:101], v[84:85]
	v_mov_b64_e32 v[98:99], v[82:83]
	s_nop 1
	v_mfma_f32_32x32x16_f16 v[98:113], v[150:153], v[142:145], v[98:113]
	v_mfma_f32_32x32x16_f16 v[98:113], v[158:161], v[138:141], v[98:113]
	v_mfma_f32_32x32x16_f16 v[98:113], v[162:165], v[134:137], v[98:113]
	v_mfma_f32_32x32x16_f16 v[98:113], v[170:173], v[130:133], v[98:113]
	ds_read_b64_tr_b16 v[170:171], v2 offset:24576
	ds_read_b64_tr_b16 v[172:173], v16 offset:24576
	ds_read_b64_tr_b16 v[152:153], v16 offset:28672
	ds_read_b64_tr_b16 v[150:151], v2 offset:28672
	ds_read_b64_tr_b16 v[182:183], v17 offset:24576
	ds_read_b64_tr_b16 v[184:185], v186 offset:24576
	ds_read_b64_tr_b16 v[160:161], v186 offset:28672
	ds_read_b64_tr_b16 v[158:159], v17 offset:28672
	ds_read_b64_tr_b16 v[186:187], v190 offset:24576
	ds_read_b64_tr_b16 v[188:189], v191 offset:24576
	ds_read_b64_tr_b16 v[164:165], v191 offset:28672
	ds_read_b64_tr_b16 v[162:163], v190 offset:28672
	v_max3_f32 v17, v98, v99, v100
	v_max3_f32 v190, v101, v102, v103
	v_max3_f32 v2, v114, v115, v116
	v_max3_f32 v16, v117, v118, v119
	s_nop 0
	v_max3_f32 v17, v17, v104, v105
	v_max3_f32 v190, v190, v106, v107
	v_max3_f32 v2, v2, v120, v121
	v_max3_f32 v16, v16, v122, v123
	s_nop 0
	v_max3_f32 v17, v17, v108, v109
	v_max3_f32 v190, v190, v110, v111
	v_max3_f32 v2, v2, v124, v125
	v_max3_f32 v16, v16, v126, v127
	s_nop 0
	v_max3_f32 v17, v17, v112, v113
	v_max_f32_e32 v190, v190, v190
	v_max_f32_e32 v17, v17, v17
	v_max3_f32 v2, v2, v128, v129
	v_max_f32_e32 v17, v17, v190
	v_max3_f32 v2, v2, v16, v17
	v_and_b32_e32 v17, 64, v215
	v_xor_b32_e32 v16, 32, v215
	v_add_u32_e32 v17, 64, v17
	v_cmp_lt_i32_e32 vcc, v16, v17
	ds_read_b64_tr_b16 v[194:195], v233 offset:24576
	ds_read_b64_tr_b16 v[196:197], v192 offset:24576
	ds_read_b64_tr_b16 v[192:193], v192 offset:28672
	ds_read_b64_tr_b16 v[190:191], v233 offset:28672
	v_cndmask_b32_e32 v16, v215, v16, vcc
	v_lshlrev_b32_e32 v217, 2, v16
	v_mov_b32_e32 v16, v2
	v_mov_b32_e32 v17, v2
	s_nop 1
	v_permlane32_swap_b32_e32 v16, v17
	v_max3_f32 v17, v2, v16, v17
	v_cmp_ge_f32_e32 vcc, s70, v17
	s_nop 1
	v_cndmask_b32_e64 v2, 0, 1, vcc
	v_cmp_eq_f32_e32 vcc, s72, v17
	s_nop 1
	v_cndmask_b32_e64 v16, 0, 1, vcc
	v_cndmask_b32_e64 v2, v16, v2, s[4:5]
	v_and_b32_e32 v2, 1, v2
	v_cmp_ne_u32_e32 vcc, 0, v2
	s_cmp_eq_u64 vcc, exec
	v_mov_b32_e32 v2, 0
	s_cbranch_scc1 .LBB0_568
	s_xor_b64 s[6:7], s[4:5], -1
	s_and_saveexec_b64 s[8:9], s[6:7]
	s_xor_b64 s[6:7], exec, s[8:9]
	s_cbranch_execz .LBB0_565
	v_cmp_lg_f32_e32 vcc, s72, v17
	s_mov_b64 s[4:5], 0
	v_mov_b32_e32 v2, 0
	s_and_saveexec_b64 s[8:9], vcc
	s_mov_b64 s[4:5], exec
	v_mov_b32_e32 v2, v17
	s_or_b64 exec, exec, s[8:9]
